# baseline (speedup 1.0000x reference)
_Z9tg_kernelILi64ELi8ELi3ELb0EEvPKDF16_iS1_iPviPKf:
	s_load_dwordx2 s[4:5], s[0:1], 0x0
	s_load_dword s7, s[0:1], 0x8
	s_load_dwordx2 s[12:13], s[0:1], 0x10
	s_load_dword s6, s[0:1], 0x18
	v_readfirstlane_b32 s9, v0
	s_lshr_b32 s8, s9, 6
	s_lshl_b32 s10, s3, 6
	s_lshl_b32 s11, s2, 7
	v_bfe_u32 v1, v0, 3, 3
	v_bitop3_b32 v8, v1, v0, 7 bitop3:0x78
	v_or_b32_e32 v2, s10, v1
	s_lshl_b32 s14, s8, 3
	v_or_b32_e32 v1, s11, v1
	v_add_u32_e32 v1, s14, v1
	s_waitcnt lgkmcnt(0)
	v_mad_i64_i32 v[4:5], s[2:3], v1, s6, 0
	v_add_u32_e32 v2, s14, v2
	v_lshl_add_u64 v[6:7], v[4:5], 1, s[12:13]
	v_lshlrev_b32_e32 v4, 4, v8
	v_mov_b32_e32 v5, 0
	v_add_u32_e32 v1, 64, v1
	v_mad_i64_i32 v[2:3], s[2:3], v2, s7, 0
	v_lshl_add_u64 v[50:51], v[6:7], 0, v[4:5]
	v_mad_i64_i32 v[6:7], s[2:3], v1, s6, 0
	s_lshl_b32 s2, s8, 10
	v_lshl_add_u64 v[2:3], v[2:3], 1, s[4:5]
	s_add_i32 s14, s2, 0
	v_lshl_add_u64 v[54:55], v[2:3], 0, v[4:5]
	s_mov_b32 m0, s14
	v_lshl_add_u64 v[6:7], v[6:7], 1, s[12:13]
	global_load_lds_dwordx4 v[54:55], off
	s_add_i32 m0, s14, 0x2000
	v_lshl_add_u64 v[52:53], v[6:7], 0, v[4:5]
	global_load_lds_dwordx4 v[50:51], off
	s_add_i32 m0, s14, 0x4000
	s_ashr_i32 s7, s6, 31
	global_load_lds_dwordx4 v[52:53], off
	v_mov_b64_e32 v[2:3], 0x80
	v_cmp_lt_i64_e32 vcc, s[6:7], v[2:3]
	s_mov_b64 s[2:3], 0x80
	v_and_b32_e32 v2, 63, v0
	s_cbranch_vccnz .LBB7_2
	v_lshl_add_u64 v[6:7], v[54:55], 0, s[2:3]
	s_add_i32 m0, s14, 0x6000
	s_nop 0
	global_load_lds_dwordx4 v[6:7], off
	s_add_i32 m0, s14, 0x8000
	v_lshl_add_u64 v[6:7], v[50:51], 0, s[2:3]
	global_load_lds_dwordx4 v[6:7], off
	v_lshl_add_u64 v[6:7], v[52:53], 0, s[2:3]
	s_add_i32 m0, s14, 0xa000
	s_nop 0
	global_load_lds_dwordx4 v[6:7], off
	s_mov_b64 s[2:3], 256
	v_lshl_add_u64 v[6:7], v[54:55], 0, s[2:3]
	s_add_i32 m0, s14, 0xc000
	s_nop 0
	global_load_lds_dwordx4 v[6:7], off
	s_add_i32 m0, s14, 0xe000
	v_lshl_add_u64 v[6:7], v[50:51], 0, s[2:3]
	global_load_lds_dwordx4 v[6:7], off
	v_lshl_add_u64 v[6:7], v[52:53], 0, s[2:3]
	s_add_i32 m0, s14, 0x10000
	s_nop 0
	global_load_lds_dwordx4 v[6:7], off
	s_mov_b64 s[2:3], 384
	v_lshl_add_u64 v[6:7], v[54:55], 0, s[2:3]
	s_add_i32 m0, s14, 0x12000
	s_nop 0
	global_load_lds_dwordx4 v[6:7], off
	s_add_i32 m0, s14, 0x14000
	v_lshl_add_u64 v[6:7], v[50:51], 0, s[2:3]
	global_load_lds_dwordx4 v[6:7], off
	v_lshl_add_u64 v[6:7], v[52:53], 0, s[2:3]
	s_add_i32 m0, s14, 0x16000
	s_nop 0
	global_load_lds_dwordx4 v[6:7], off

.Ltk7_ns:
	s_add_u32 s24, s24, 256
	s_add_i32 s20, s20, 2
	s_cmp_lt_i32 s20, s15
	s_cbranch_scc1 .Ltk7_top
.LBB7_11:
	v_lshlrev_b32_e32 v0, 2, v56
	v_lshl_or_b32 v0, s13, 5, v0
	v_or_b32_e32 v26, s11, v0
	v_ashrrev_i32_e32 v27, 31, v26
	s_waitcnt lgkmcnt(0)
	v_lshl_add_u64 v[28:29], v[26:27], 2, s[4:5]
	global_load_dwordx4 v[18:21], v[28:29], off
	global_load_dwordx4 v[22:25], v[28:29], off offset:64
	s_load_dword s4, s[0:1], 0x28
	s_lshl_b32 s0, s12, 5
	s_add_i32 s0, s0, s10
	v_or_b32_e32 v28, s0, v1
	v_or_b32_e32 v29, 16, v28
	v_lshl_add_u64 v[0:1], v[26:27], 1, s[2:3]
	s_waitcnt lgkmcnt(0)
	v_mad_i64_i32 v[26:27], s[0:1], v28, s4, 0
	v_mad_i64_i32 v[28:29], s[0:1], v29, s4, 0
	v_lshl_add_u64 v[26:27], v[26:27], 1, v[0:1]
	v_lshl_add_u64 v[0:1], v[28:29], 1, v[0:1]
	s_waitcnt vmcnt(0)
	v_pk_add_f32 v[12:13], v[20:21], v[12:13]
	v_pk_add_f32 v[10:11], v[18:19], v[10:11]
	v_pk_add_f32 v[16:17], v[20:21], v[16:17]
	v_pk_add_f32 v[14:15], v[18:19], v[14:15]
	v_pk_add_f32 v[8:9], v[24:25], v[8:9]
	v_pk_add_f32 v[6:7], v[22:23], v[6:7]
	v_pk_add_f32 v[4:5], v[24:25], v[4:5]
	v_pk_add_f32 v[2:3], v[22:23], v[2:3]
	v_cvt_pk_f16_f32 v13, v12, v13
	v_cvt_pk_f16_f32 v12, v10, v11
	v_cvt_pk_f16_f32 v11, v16, v17
	v_cvt_pk_f16_f32 v10, v14, v15
	v_cvt_pk_f16_f32 v9, v8, v9
	v_cvt_pk_f16_f32 v8, v6, v7
	v_cvt_pk_f16_f32 v5, v4, v5
	v_cvt_pk_f16_f32 v4, v2, v3
	global_store_dwordx2 v[26:27], v[12:13], off
	global_store_dwordx2 v[0:1], v[10:11], off
	global_store_dwordx2 v[26:27], v[8:9], off offset:32
	global_store_dwordx2 v[0:1], v[4:5], off offset:32
	s_endpgm
	.p2align	8

	.amdhsa_kernel _Z9tg_kernelILi64ELi8ELi3ELb0EEvPKDF16_iS1_iPviPKf
		.amdhsa_group_segment_fixed_size 73728
		.amdhsa_private_segment_fixed_size 0
		.amdhsa_kernarg_size 56
		.amdhsa_user_sgpr_count 2
		.amdhsa_user_sgpr_dispatch_ptr 0
		.amdhsa_user_sgpr_queue_ptr 0
		.amdhsa_user_sgpr_kernarg_segment_ptr 1
		.amdhsa_user_sgpr_dispatch_id 0
		.amdhsa_user_sgpr_kernarg_preload_length 0
		.amdhsa_user_sgpr_kernarg_preload_offset 0
		.amdhsa_user_sgpr_private_segment_size 0
		.amdhsa_uses_dynamic_stack 0
		.amdhsa_enable_private_segment 0
		.amdhsa_system_sgpr_workgroup_id_x 1
		.amdhsa_system_sgpr_workgroup_id_y 1
		.amdhsa_system_sgpr_workgroup_id_z 0
		.amdhsa_system_sgpr_workgroup_info 0
		.amdhsa_system_vgpr_workitem_id 0
		.amdhsa_next_free_vgpr 128
		.amdhsa_next_free_sgpr 32
		.amdhsa_accum_offset 128
		.amdhsa_reserve_vcc 1
		.amdhsa_float_round_mode_32 0
		.amdhsa_float_round_mode_16_64 0
		.amdhsa_float_denorm_mode_32 3
		.amdhsa_float_denorm_mode_16_64 3
		.amdhsa_dx10_clamp 1
		.amdhsa_ieee_mode 1
		.amdhsa_fp16_overflow 0
		.amdhsa_tg_split 0
		.amdhsa_exception_fp_ieee_invalid_op 0
		.amdhsa_exception_fp_denorm_src 0
		.amdhsa_exception_fp_ieee_div_zero 0
		.amdhsa_exception_fp_ieee_overflow 0
		.amdhsa_exception_fp_ieee_underflow 0
		.amdhsa_exception_fp_ieee_inexact 0
		.amdhsa_exception_int_div_zero 0
	.end_amdhsa_kernel

_Z9tg_kernelILi64ELi8ELi4ELb0EEvPKDF16_iS1_iPviPKf:
	s_load_dwordx2 s[4:5], s[0:1], 0x0
	s_load_dword s7, s[0:1], 0x8
	s_load_dwordx2 s[12:13], s[0:1], 0x10
	s_load_dword s6, s[0:1], 0x18
	v_readfirstlane_b32 s9, v0
	s_lshr_b32 s8, s9, 6
	s_lshl_b32 s10, s3, 6
	v_bfe_u32 v1, v0, 3, 3
	s_lshl_b32 s11, s2, 7
	v_or_b32_e32 v2, s10, v1
	s_lshl_b32 s14, s8, 3
	v_bitop3_b32 v8, v1, v0, 7 bitop3:0x78
	v_add_u32_e32 v2, s14, v2
	v_or_b32_e32 v1, s11, v1
	s_waitcnt lgkmcnt(0)
	v_mad_i64_i32 v[2:3], s[2:3], v2, s7, 0
	v_add_u32_e32 v1, s14, v1
	v_lshl_add_u64 v[4:5], v[2:3], 1, s[4:5]
	v_mad_i64_i32 v[2:3], s[2:3], v1, s6, 0
	v_lshl_add_u64 v[6:7], v[2:3], 1, s[12:13]
	v_lshlrev_b32_e32 v2, 4, v8
	v_mov_b32_e32 v3, 0
	v_add_u32_e32 v1, 64, v1
	v_lshl_add_u64 v[48:49], v[6:7], 0, v[2:3]
	v_mad_i64_i32 v[6:7], s[2:3], v1, s6, 0
	s_lshl_b32 s2, s8, 10
	s_add_i32 s14, s2, 0
	v_lshl_add_u64 v[52:53], v[4:5], 0, v[2:3]
	s_mov_b32 m0, s14
	v_lshl_add_u64 v[6:7], v[6:7], 1, s[12:13]
	global_load_lds_dwordx4 v[52:53], off
	s_add_i32 m0, s14, 0x2000
	v_lshl_add_u64 v[50:51], v[6:7], 0, v[2:3]
	global_load_lds_dwordx4 v[48:49], off
	s_add_i32 m0, s14, 0x4000
	s_ashr_i32 s7, s6, 31
	global_load_lds_dwordx4 v[50:51], off
	v_mov_b64_e32 v[4:5], 0x80
	v_cmp_lt_i64_e32 vcc, s[6:7], v[4:5]
	s_mov_b64 s[2:3], 0x80
	v_and_b32_e32 v1, 63, v0
	s_cbranch_vccnz .LBB11_2
	v_lshl_add_u64 v[4:5], v[52:53], 0, s[2:3]
	s_add_i32 m0, s14, 0x6000
	s_nop 0
	global_load_lds_dwordx4 v[4:5], off
	s_add_i32 m0, s14, 0x8000
	v_lshl_add_u64 v[4:5], v[48:49], 0, s[2:3]
	global_load_lds_dwordx4 v[4:5], off
	v_lshl_add_u64 v[4:5], v[50:51], 0, s[2:3]
	s_add_i32 m0, s14, 0xa000
	s_nop 0
	global_load_lds_dwordx4 v[4:5], off
	s_mov_b64 s[2:3], 256
	v_lshl_add_u64 v[4:5], v[52:53], 0, s[2:3]
	s_add_i32 m0, s14, 0xc000
	s_nop 0
	global_load_lds_dwordx4 v[4:5], off
	s_add_i32 m0, s14, 0xe000
	v_lshl_add_u64 v[4:5], v[48:49], 0, s[2:3]
	global_load_lds_dwordx4 v[4:5], off
	v_lshl_add_u64 v[4:5], v[50:51], 0, s[2:3]
	s_add_i32 m0, s14, 0x10000
	s_nop 0
	global_load_lds_dwordx4 v[4:5], off
	s_mov_b64 s[2:3], 384
	v_lshl_add_u64 v[4:5], v[52:53], 0, s[2:3]
	s_add_i32 m0, s14, 0x12000
	s_nop 0
	global_load_lds_dwordx4 v[4:5], off
	s_add_i32 m0, s14, 0x14000
	v_lshl_add_u64 v[4:5], v[48:49], 0, s[2:3]
	global_load_lds_dwordx4 v[4:5], off
	v_lshl_add_u64 v[4:5], v[50:51], 0, s[2:3]
	s_add_i32 m0, s14, 0x16000
	s_nop 0
	global_load_lds_dwordx4 v[4:5], off
.LBB11_2:
	s_load_dwordx2 s[2:3], s[0:1], 0x20
	s_load_dwordx2 s[4:5], s[0:1], 0x30
	s_lshr_b32 s12, s9, 8
	s_and_b32 s13, s8, 3
	v_and_b32_e32 v54, 7, v0
	v_and_b32_e32 v55, 15, v0
	v_lshrrev_b32_e32 v56, 4, v1
	s_cmp_lt_i32 s6, 64
	v_mov_b32_e32 v2, 0
	v_mov_b32_e32 v1, 0
	v_mov_b32_e32 v0, 0
	v_mov_b32_e32 v11, 0
	v_mov_b32_e32 v10, 0
	v_mov_b32_e32 v9, 0
	v_mov_b32_e32 v8, 0
	v_mov_b32_e32 v7, 0
	v_mov_b32_e32 v6, 0
	v_mov_b32_e32 v5, 0
	v_mov_b32_e32 v4, 0
	v_mov_b32_e32 v15, 0
	v_mov_b32_e32 v14, 0
	v_mov_b32_e32 v13, 0
	v_mov_b32_e32 v12, 0
	s_cbranch_scc1 .LBB11_11
	v_xor_b32_e32 v0, v56, v54
	s_lshr_b32 s7, s7, 26
	v_lshlrev_b32_e32 v57, 4, v0
	v_lshlrev_b32_e32 v0, 7, v55
	v_bitop3_b32 v1, v56, v54, 4 bitop3:0x36
	s_add_i32 s6, s6, s7
	v_mov_b32_e32 v12, 0
	s_mov_b32 s7, 0
	v_lshl_or_b32 v58, s12, 12, v0
	v_lshlrev_b32_e32 v59, 4, v1
	v_lshl_or_b32 v60, s13, 12, v0
	s_ashr_i32 s15, s6, 6
	s_movk_i32 s6, 0x80
	s_mov_b32 s18, s7
	s_mov_b32 s16, s7
	v_mov_b32_e32 v13, v12
	v_mov_b32_e32 v14, v12
	v_mov_b32_e32 v15, v12
	v_mov_b32_e32 v4, v12
	v_mov_b32_e32 v5, v12
	v_mov_b32_e32 v6, v12
	v_mov_b32_e32 v7, v12
	v_mov_b32_e32 v8, v12
	v_mov_b32_e32 v9, v12
	v_mov_b32_e32 v10, v12
	v_mov_b32_e32 v11, v12
	v_mov_b32_e32 v0, v12
	v_mov_b32_e32 v1, v12
	v_mov_b32_e32 v2, v12
	v_mov_b32_e32 v3, v12
	s_mov_b32 s20, 0
	s_mov_b32 s21, 0
	s_mov_b32 s24, 512
	s_mov_b32 s25, 0

.Ltk11_wd:
	s_mov_b32 s9, s21
	s_add_i32 s23, s21, 0x6000
	s_barrier
	v_add_u32_e32 v24, s9, v57
	v_add_u32_e32 v40, s9, v59
	v_add_u32_e32 v16, v24, v58
	v_add_u32_e32 v28, v24, v60
	v_add_u32_e32 v32, v40, v58
	v_add_u32_e32 v44, v40, v60
	ds_read_b128 v[20:23], v16
	ds_read_b128 v[16:19], v16 offset:2048
	ds_read_b128 v[24:27], v28 offset:8192
	ds_read_b128 v[28:31], v28 offset:10240
	ds_read_b128 v[36:39], v32
	ds_read_b128 v[32:35], v32 offset:2048
	ds_read_b128 v[40:43], v44 offset:8192
	ds_read_b128 v[44:47], v44 offset:10240
	v_add_u32_e32 v88, s23, v57
	v_add_u32_e32 v104, s23, v59
	v_add_u32_e32 v80, v88, v58
	v_add_u32_e32 v92, v88, v60
	v_add_u32_e32 v96, v104, v58
	v_add_u32_e32 v108, v104, v60
	ds_read_b128 v[84:87], v80
	ds_read_b128 v[80:83], v80 offset:2048
	ds_read_b128 v[88:91], v92 offset:8192
	ds_read_b128 v[92:95], v92 offset:10240
	ds_read_b128 v[100:103], v96
	ds_read_b128 v[96:99], v96 offset:2048
	ds_read_b128 v[104:107], v108 offset:8192
	ds_read_b128 v[108:111], v108 offset:10240
	s_add_i32 s22, s20, 4
	s_cmp_ge_i32 s22, s15
	s_cbranch_scc1 .Ltk11_noi
	s_add_i32 s26, s21, 0x18000
	s_cmp_ge_u32 s26, 0x24000
	s_cbranch_scc0 .Ltk11_nw
	s_sub_i32 s26, s26, 0x24000
.Ltk11_nw:
	v_lshl_add_u64 v[62:63], v[52:53], 0, s[24:25]
	s_add_i32 m0, s14, s26
	s_nop 0
	global_load_lds_dwordx4 v[62:63], off
	s_add_i32 s27, s26, 0x2000
	v_lshl_add_u64 v[62:63], v[48:49], 0, s[24:25]
	s_add_i32 m0, s14, s27
	s_nop 0
	global_load_lds_dwordx4 v[62:63], off
	s_add_i32 s27, s26, 0x4000
	v_lshl_add_u64 v[62:63], v[50:51], 0, s[24:25]
	s_add_i32 m0, s14, s27
	s_nop 0
	global_load_lds_dwordx4 v[62:63], off
	s_add_u32 s28, s24, 128
	s_addc_u32 s29, s25, 0
	s_add_i32 s26, s26, 0x6000
	v_lshl_add_u64 v[62:63], v[52:53], 0, s[28:29]
	s_add_i32 m0, s14, s26
	s_nop 0
	global_load_lds_dwordx4 v[62:63], off
	s_add_i32 s27, s26, 0x2000
	v_lshl_add_u64 v[62:63], v[48:49], 0, s[28:29]
	s_add_i32 m0, s14, s27
	s_nop 0
	global_load_lds_dwordx4 v[62:63], off
	s_add_i32 s27, s26, 0x4000
	v_lshl_add_u64 v[62:63], v[50:51], 0, s[28:29]
	s_add_i32 m0, s14, s27
	s_nop 0
	global_load_lds_dwordx4 v[62:63], off
.Ltk11_noi:
	s_setprio 1
	s_waitcnt lgkmcnt(0)
	v_mfma_f32_16x16x32_f16 v[12:15], v[24:27], v[20:23], v[12:15]
	v_mfma_f32_16x16x32_f16 v[4:7], v[28:31], v[20:23], v[4:7]
	v_mfma_f32_16x16x32_f16 v[8:11], v[24:27], v[16:19], v[8:11]
	v_mfma_f32_16x16x32_f16 v[0:3], v[28:31], v[16:19], v[0:3]
	v_mfma_f32_16x16x32_f16 v[12:15], v[40:43], v[36:39], v[12:15]
	v_mfma_f32_16x16x32_f16 v[4:7], v[44:47], v[36:39], v[4:7]
	v_mfma_f32_16x16x32_f16 v[8:11], v[40:43], v[32:35], v[8:11]
	v_mfma_f32_16x16x32_f16 v[0:3], v[44:47], v[32:35], v[0:3]
	v_mfma_f32_16x16x32_f16 v[12:15], v[88:91], v[84:87], v[12:15]
	v_mfma_f32_16x16x32_f16 v[4:7], v[92:95], v[84:87], v[4:7]
	v_mfma_f32_16x16x32_f16 v[8:11], v[88:91], v[80:83], v[8:11]
	v_mfma_f32_16x16x32_f16 v[0:3], v[92:95], v[80:83], v[0:3]
	v_mfma_f32_16x16x32_f16 v[12:15], v[104:107], v[100:103], v[12:15]
	v_mfma_f32_16x16x32_f16 v[4:7], v[108:111], v[100:103], v[4:7]
	v_mfma_f32_16x16x32_f16 v[8:11], v[104:107], v[96:99], v[8:11]
	v_mfma_f32_16x16x32_f16 v[0:3], v[108:111], v[96:99], v[0:3]
	s_setprio 0
	s_add_i32 s21, s21, 0xc000
	s_cmp_ge_u32 s21, 0x24000
	s_cbranch_scc0 .Ltk11_ns
	s_mov_b32 s21, 0
.Ltk11_ns:
	s_add_u32 s24, s24, 256
	s_add_i32 s20, s20, 2
	s_cmp_lt_i32 s20, s15
	s_cbranch_scc1 .Ltk11_top
.LBB11_11:
	v_lshlrev_b32_e32 v16, 2, v56
	v_lshl_or_b32 v16, s13, 5, v16
	v_or_b32_e32 v34, s11, v16
	v_ashrrev_i32_e32 v35, 31, v34
	s_waitcnt lgkmcnt(0)
	v_lshl_add_u64 v[20:21], v[34:35], 2, s[4:5]
	global_load_dwordx4 v[16:19], v[20:21], off
	v_mbcnt_lo_u32_b32 v22, -1, 0
	v_mbcnt_hi_u32_b32 v22, -1, v22
	v_and_b32_e32 v24, 64, v22
	v_xor_b32_e32 v23, 1, v22
	v_add_u32_e32 v24, 64, v24
	v_xor_b32_e32 v25, 2, v22
	v_cmp_lt_i32_e32 vcc, v23, v24
	v_xor_b32_e32 v26, 4, v22
	s_load_dword s4, s[0:1], 0x28
	v_cndmask_b32_e32 v23, v22, v23, vcc
	v_cmp_lt_i32_e32 vcc, v25, v24
	s_lshl_b32 s0, s12, 5
	s_add_i32 s0, s0, s10
	v_cndmask_b32_e32 v25, v22, v25, vcc
	v_cmp_lt_i32_e32 vcc, v26, v24
	s_waitcnt vmcnt(0)
	v_pk_add_f32 v[14:15], v[18:19], v[14:15]
	v_pk_add_f32 v[12:13], v[16:17], v[12:13]
	v_cndmask_b32_e32 v24, v22, v26, vcc
	v_lshlrev_b32_e32 v22, 2, v23
	v_max_f32_e32 v12, 0, v12
	v_max_f32_e32 v13, 0, v13
	v_max_f32_e32 v23, 0, v14
	v_max_f32_e32 v15, 0, v15
	ds_bpermute_b32 v26, v22, v12
	ds_bpermute_b32 v27, v22, v13
	ds_bpermute_b32 v28, v22, v23
	ds_bpermute_b32 v29, v22, v15
	v_lshlrev_b32_e32 v14, 2, v25
	s_waitcnt lgkmcnt(0)
	v_max_f32_e32 v25, v26, v26
	v_max_f32_e32 v26, v27, v27
	v_max_f32_e32 v27, v28, v28
	v_max_f32_e32 v28, v29, v29
	v_max_f32_e32 v12, v12, v25
	v_max_f32_e32 v13, v13, v26
	v_max_f32_e32 v23, v23, v27
	v_max_f32_e32 v28, v15, v28
	ds_bpermute_b32 v25, v14, v12
	ds_bpermute_b32 v26, v14, v13
	ds_bpermute_b32 v27, v14, v23
	ds_bpermute_b32 v29, v14, v28
	v_lshlrev_b32_e32 v15, 2, v24
	s_waitcnt lgkmcnt(3)
	v_max_f32_e32 v24, v25, v25
	s_waitcnt lgkmcnt(2)
	v_max_f32_e32 v25, v26, v26
	s_waitcnt lgkmcnt(1)
	v_max_f32_e32 v30, v27, v27
	s_waitcnt lgkmcnt(0)
	v_max_f32_e32 v29, v29, v29
	v_max_f32_e32 v27, v12, v24
	v_max_f32_e32 v26, v13, v25
	v_max_f32_e32 v25, v23, v30
	v_max_f32_e32 v31, v28, v29
	ds_bpermute_b32 v30, v15, v27
	ds_bpermute_b32 v29, v15, v26
	ds_bpermute_b32 v28, v15, v25
	ds_bpermute_b32 v32, v15, v31
	v_or_b32_e32 v24, s0, v55
	v_cmp_eq_u32_e32 vcc, 0, v54
	v_lshl_add_u64 v[12:13], v[34:35], 1, s[2:3]
	v_ashrrev_i32_e32 v23, 3, v24
	s_and_saveexec_b64 s[0:1], vcc
	s_cbranch_execz .LBB11_13
	s_waitcnt lgkmcnt(3)
	v_max_f32_e32 v30, v30, v30
	v_max_f32_e32 v27, v27, v27
	v_max_f32_e32 v30, v27, v30
	s_waitcnt lgkmcnt(2)
	v_max_f32_e32 v27, v29, v29
	v_max_f32_e32 v26, v26, v26
	s_waitcnt lgkmcnt(0)
	v_max_f32_e32 v32, v32, v32
	v_max_f32_e32 v31, v31, v31
	v_max_f32_e32 v26, v26, v27
	v_max_f32_e32 v27, v28, v28
	v_max_f32_e32 v25, v25, v25
	v_max_f32_e32 v31, v31, v32
	v_max_f32_e32 v25, v25, v27
	v_mad_i64_i32 v[28:29], s[2:3], v23, s4, 0
	v_cvt_pk_f16_f32 v27, v25, v31
	v_cvt_pk_f16_f32 v26, v30, v26
	v_lshl_add_u64 v[28:29], v[28:29], 1, v[12:13]
	global_store_dwordx2 v[28:29], v[26:27], off

	.amdhsa_kernel _Z9tg_kernelILi64ELi8ELi4ELb0EEvPKDF16_iS1_iPviPKf
		.amdhsa_group_segment_fixed_size 73728
		.amdhsa_private_segment_fixed_size 0
		.amdhsa_kernarg_size 56
		.amdhsa_user_sgpr_count 2
		.amdhsa_user_sgpr_dispatch_ptr 0
		.amdhsa_user_sgpr_queue_ptr 0
		.amdhsa_user_sgpr_kernarg_segment_ptr 1
		.amdhsa_user_sgpr_dispatch_id 0
		.amdhsa_user_sgpr_kernarg_preload_length 0
		.amdhsa_user_sgpr_kernarg_preload_offset 0
		.amdhsa_user_sgpr_private_segment_size 0
		.amdhsa_uses_dynamic_stack 0
		.amdhsa_enable_private_segment 0
		.amdhsa_system_sgpr_workgroup_id_x 1
		.amdhsa_system_sgpr_workgroup_id_y 1
		.amdhsa_system_sgpr_workgroup_id_z 0
		.amdhsa_system_sgpr_workgroup_info 0
		.amdhsa_system_vgpr_workitem_id 0
		.amdhsa_next_free_vgpr 128
		.amdhsa_next_free_sgpr 32
		.amdhsa_accum_offset 128
		.amdhsa_reserve_vcc 1
		.amdhsa_float_round_mode_32 0
		.amdhsa_float_round_mode_16_64 0
		.amdhsa_float_denorm_mode_32 3
		.amdhsa_float_denorm_mode_16_64 3
		.amdhsa_dx10_clamp 1
		.amdhsa_ieee_mode 1
		.amdhsa_fp16_overflow 0
		.amdhsa_tg_split 0
		.amdhsa_exception_fp_ieee_invalid_op 0
		.amdhsa_exception_fp_denorm_src 0
		.amdhsa_exception_fp_ieee_div_zero 0
		.amdhsa_exception_fp_ieee_overflow 0
		.amdhsa_exception_fp_ieee_underflow 0
		.amdhsa_exception_fp_ieee_inexact 0
		.amdhsa_exception_int_div_zero 0
	.end_amdhsa_kernel

_Z9tg_kernelILi64ELi8ELi2ELb0EEvPKDF16_iS1_iPviPKf:
	s_load_dwordx2 s[10:11], s[0:1], 0x0
	s_load_dword s5, s[0:1], 0x8
	s_load_dwordx2 s[12:13], s[0:1], 0x10
	s_load_dword s4, s[0:1], 0x18
	v_readfirstlane_b32 s8, v0
	s_lshr_b32 s9, s8, 6
	s_lshl_b32 s6, s3, 6
	s_lshl_b32 s7, s2, 7
	v_bfe_u32 v1, v0, 3, 3
	v_bitop3_b32 v8, v1, v0, 7 bitop3:0x78
	v_or_b32_e32 v2, s6, v1
	s_lshl_b32 s14, s9, 3
	v_or_b32_e32 v1, s7, v1
	v_add_u32_e32 v1, s14, v1
	s_waitcnt lgkmcnt(0)
	v_mad_i64_i32 v[4:5], s[2:3], v1, s4, 0
	v_add_u32_e32 v2, s14, v2
	v_lshl_add_u64 v[6:7], v[4:5], 1, s[12:13]
	v_lshlrev_b32_e32 v4, 4, v8
	v_mov_b32_e32 v5, 0
	v_add_u32_e32 v1, 64, v1
	v_mad_i64_i32 v[2:3], s[2:3], v2, s5, 0
	v_lshl_add_u64 v[50:51], v[6:7], 0, v[4:5]
	v_mad_i64_i32 v[6:7], s[2:3], v1, s4, 0
	s_lshl_b32 s2, s9, 10
	v_lshl_add_u64 v[2:3], v[2:3], 1, s[10:11]
	s_add_i32 s10, s2, 0
	v_lshl_add_u64 v[54:55], v[2:3], 0, v[4:5]
	s_mov_b32 m0, s10
	v_lshl_add_u64 v[6:7], v[6:7], 1, s[12:13]
	global_load_lds_dwordx4 v[54:55], off
	s_add_i32 m0, s10, 0x2000
	v_lshl_add_u64 v[52:53], v[6:7], 0, v[4:5]
	global_load_lds_dwordx4 v[50:51], off
	s_add_i32 m0, s10, 0x4000
	s_ashr_i32 s5, s4, 31
	global_load_lds_dwordx4 v[52:53], off
	v_mov_b64_e32 v[2:3], 0x80
	v_cmp_lt_i64_e32 vcc, s[4:5], v[2:3]
	s_mov_b64 s[2:3], 0x80
	v_and_b32_e32 v2, 63, v0
	s_cbranch_vccnz .LBB12_2
	v_lshl_add_u64 v[6:7], v[54:55], 0, s[2:3]
	s_add_i32 m0, s10, 0x6000
	s_nop 0
	global_load_lds_dwordx4 v[6:7], off
	s_add_i32 m0, s10, 0x8000
	v_lshl_add_u64 v[6:7], v[50:51], 0, s[2:3]
	global_load_lds_dwordx4 v[6:7], off
	v_lshl_add_u64 v[6:7], v[52:53], 0, s[2:3]
	s_add_i32 m0, s10, 0xa000
	s_nop 0
	global_load_lds_dwordx4 v[6:7], off
	s_mov_b64 s[2:3], 256
	v_lshl_add_u64 v[6:7], v[54:55], 0, s[2:3]
	s_add_i32 m0, s10, 0xc000
	s_nop 0
	global_load_lds_dwordx4 v[6:7], off
	s_add_i32 m0, s10, 0xe000
	v_lshl_add_u64 v[6:7], v[50:51], 0, s[2:3]
	global_load_lds_dwordx4 v[6:7], off
	v_lshl_add_u64 v[6:7], v[52:53], 0, s[2:3]
	s_add_i32 m0, s10, 0x10000
	s_nop 0
	global_load_lds_dwordx4 v[6:7], off
	s_mov_b64 s[2:3], 384
	v_lshl_add_u64 v[6:7], v[54:55], 0, s[2:3]
	s_add_i32 m0, s10, 0x12000
	s_nop 0
	global_load_lds_dwordx4 v[6:7], off
	s_add_i32 m0, s10, 0x14000
	v_lshl_add_u64 v[6:7], v[50:51], 0, s[2:3]
	global_load_lds_dwordx4 v[6:7], off
	v_lshl_add_u64 v[6:7], v[52:53], 0, s[2:3]
	s_add_i32 m0, s10, 0x16000
	s_nop 0
	global_load_lds_dwordx4 v[6:7], off
.LBB12_2:
	s_lshr_b32 s8, s8, 8
	s_and_b32 s9, s9, 3
	v_and_b32_e32 v1, 15, v0
	v_lshrrev_b32_e32 v56, 4, v2
	s_cmp_lt_i32 s4, 64
	v_mov_b32_e32 v4, 0
	v_mov_b32_e32 v3, 0
	v_mov_b32_e32 v2, 0
	v_mov_b32_e32 v17, 0
	v_mov_b32_e32 v16, 0
	v_mov_b32_e32 v15, 0
	v_mov_b32_e32 v14, 0
	v_mov_b32_e32 v9, 0
	v_mov_b32_e32 v8, 0
	v_mov_b32_e32 v7, 0
	v_mov_b32_e32 v6, 0
	v_mov_b32_e32 v13, 0
	v_mov_b32_e32 v12, 0
	v_mov_b32_e32 v11, 0
	v_mov_b32_e32 v10, 0
	s_cbranch_scc1 .LBB12_11
	v_and_b32_e32 v2, 7, v0
	s_lshr_b32 s2, s5, 26
	v_xor_b32_e32 v0, v56, v2
	v_lshlrev_b32_e32 v3, 7, v1
	v_bitop3_b32 v2, v56, v2, 4 bitop3:0x36
	s_add_i32 s2, s4, s2
	v_mov_b32_e32 v10, 0
	s_mov_b32 s3, 0
	v_lshlrev_b32_e32 v0, 4, v0
	v_lshl_or_b32 v57, s8, 12, v3
	v_lshlrev_b32_e32 v58, 4, v2
	v_lshl_or_b32 v59, s9, 12, v3
	s_ashr_i32 s11, s2, 6
	s_movk_i32 s2, 0x80
	s_mov_b32 s14, s3
	s_mov_b32 s12, s3
	v_mov_b32_e32 v11, v10
	v_mov_b32_e32 v12, v10
	v_mov_b32_e32 v13, v10
	v_mov_b32_e32 v6, v10
	v_mov_b32_e32 v7, v10
	v_mov_b32_e32 v8, v10
	v_mov_b32_e32 v9, v10
	v_mov_b32_e32 v14, v10
	v_mov_b32_e32 v15, v10
	v_mov_b32_e32 v16, v10
	v_mov_b32_e32 v17, v10
	v_mov_b32_e32 v2, v10
	v_mov_b32_e32 v3, v10
	v_mov_b32_e32 v4, v10
	v_mov_b32_e32 v5, v10
	s_mov_b32 s20, 0
	s_mov_b32 s21, 0
	s_mov_b32 s24, 512
	s_mov_b32 s25, 0
.Ltk12_top:
	s_add_i32 s22, s20, 2
	s_cmp_ge_i32 s22, s11
	s_cbranch_scc1 .Ltk12_w0
	s_waitcnt vmcnt(6)
	s_branch .Ltk12_wd

.Ltk12_wd:
	s_mov_b32 s5, s21
	s_add_i32 s23, s21, 0x6000
	s_barrier
	v_add_u32_e32 v26, s5, v0
	v_add_u32_e32 v42, s5, v58
	v_add_u32_e32 v18, v26, v57
	v_add_u32_e32 v30, v26, v59
	v_add_u32_e32 v34, v42, v57
	v_add_u32_e32 v46, v42, v59
	ds_read_b128 v[22:25], v18
	ds_read_b128 v[18:21], v18 offset:2048
	ds_read_b128 v[26:29], v30 offset:8192
	ds_read_b128 v[30:33], v30 offset:10240
	ds_read_b128 v[38:41], v34
	ds_read_b128 v[34:37], v34 offset:2048
	ds_read_b128 v[42:45], v46 offset:8192
	ds_read_b128 v[46:49], v46 offset:10240
	v_add_u32_e32 v90, s23, v0
	v_add_u32_e32 v106, s23, v58
	v_add_u32_e32 v82, v90, v57
	v_add_u32_e32 v94, v90, v59
	v_add_u32_e32 v98, v106, v57
	v_add_u32_e32 v110, v106, v59
	ds_read_b128 v[86:89], v82
	ds_read_b128 v[82:85], v82 offset:2048
	ds_read_b128 v[90:93], v94 offset:8192
	ds_read_b128 v[94:97], v94 offset:10240
	ds_read_b128 v[102:105], v98
	ds_read_b128 v[98:101], v98 offset:2048
	ds_read_b128 v[106:109], v110 offset:8192
	ds_read_b128 v[110:113], v110 offset:10240
	s_add_i32 s22, s20, 4
	s_cmp_ge_i32 s22, s11
	s_cbranch_scc1 .Ltk12_noi
	s_add_i32 s26, s21, 0x18000
	s_cmp_ge_u32 s26, 0x24000
	s_cbranch_scc0 .Ltk12_nw
	s_sub_i32 s26, s26, 0x24000
.Ltk12_nw:
	v_lshl_add_u64 v[60:61], v[54:55], 0, s[24:25]
	s_add_i32 m0, s10, s26
	s_nop 0
	global_load_lds_dwordx4 v[60:61], off
	s_add_i32 s27, s26, 0x2000
	v_lshl_add_u64 v[60:61], v[50:51], 0, s[24:25]
	s_add_i32 m0, s10, s27
	s_nop 0
	global_load_lds_dwordx4 v[60:61], off
	s_add_i32 s27, s26, 0x4000
	v_lshl_add_u64 v[60:61], v[52:53], 0, s[24:25]
	s_add_i32 m0, s10, s27
	s_nop 0
	global_load_lds_dwordx4 v[60:61], off
	s_add_u32 s28, s24, 128
	s_addc_u32 s29, s25, 0
	s_add_i32 s26, s26, 0x6000
	v_lshl_add_u64 v[60:61], v[54:55], 0, s[28:29]
	s_add_i32 m0, s10, s26
	s_nop 0
	global_load_lds_dwordx4 v[60:61], off
	s_add_i32 s27, s26, 0x2000
	v_lshl_add_u64 v[60:61], v[50:51], 0, s[28:29]
	s_add_i32 m0, s10, s27
	s_nop 0
	global_load_lds_dwordx4 v[60:61], off
	s_add_i32 s27, s26, 0x4000
	v_lshl_add_u64 v[60:61], v[52:53], 0, s[28:29]
	s_add_i32 m0, s10, s27
	s_nop 0
	global_load_lds_dwordx4 v[60:61], off

.Ltk12_ns:
	s_add_u32 s24, s24, 256
	s_add_i32 s20, s20, 2
	s_cmp_lt_i32 s20, s11
	s_cbranch_scc1 .Ltk12_top

	.amdhsa_kernel _Z9tg_kernelILi64ELi8ELi2ELb0EEvPKDF16_iS1_iPviPKf
		.amdhsa_group_segment_fixed_size 73728
		.amdhsa_private_segment_fixed_size 0
		.amdhsa_kernarg_size 56
		.amdhsa_user_sgpr_count 2
		.amdhsa_user_sgpr_dispatch_ptr 0
		.amdhsa_user_sgpr_queue_ptr 0
		.amdhsa_user_sgpr_kernarg_segment_ptr 1
		.amdhsa_user_sgpr_dispatch_id 0
		.amdhsa_user_sgpr_kernarg_preload_length 0
		.amdhsa_user_sgpr_kernarg_preload_offset 0
		.amdhsa_user_sgpr_private_segment_size 0
		.amdhsa_uses_dynamic_stack 0
		.amdhsa_enable_private_segment 0
		.amdhsa_system_sgpr_workgroup_id_x 1
		.amdhsa_system_sgpr_workgroup_id_y 1
		.amdhsa_system_sgpr_workgroup_id_z 0
		.amdhsa_system_sgpr_workgroup_info 0
		.amdhsa_system_vgpr_workitem_id 0
		.amdhsa_next_free_vgpr 128
		.amdhsa_next_free_sgpr 32
		.amdhsa_accum_offset 128
		.amdhsa_reserve_vcc 1
		.amdhsa_float_round_mode_32 0
		.amdhsa_float_round_mode_16_64 0
		.amdhsa_float_denorm_mode_32 3
		.amdhsa_float_denorm_mode_16_64 3
		.amdhsa_dx10_clamp 1
		.amdhsa_ieee_mode 1
		.amdhsa_fp16_overflow 0
		.amdhsa_tg_split 0
		.amdhsa_exception_fp_ieee_invalid_op 0
		.amdhsa_exception_fp_denorm_src 0
		.amdhsa_exception_fp_ieee_div_zero 0
		.amdhsa_exception_fp_ieee_overflow 0
		.amdhsa_exception_fp_ieee_underflow 0
		.amdhsa_exception_fp_ieee_inexact 0
		.amdhsa_exception_int_div_zero 0
	.end_amdhsa_kernel

amdhsa.kernels:
  - .agpr_count:     0
    .args:
      - .offset:         0
        .size:           32
        .value_kind:     by_value
      - .address_space:  global
        .offset:         32
        .size:           8
        .value_kind:     global_buffer
      - .address_space:  global
        .offset:         40
        .size:           8
        .value_kind:     global_buffer
      - .offset:         48
        .size:           4
        .value_kind:     by_value
      - .offset:         56
        .size:           4
        .value_kind:     hidden_block_count_x
      - .offset:         60
        .size:           4
        .value_kind:     hidden_block_count_y
      - .offset:         64
        .size:           4
        .value_kind:     hidden_block_count_z
      - .offset:         68
        .size:           2
        .value_kind:     hidden_group_size_x
      - .offset:         70
        .size:           2
        .value_kind:     hidden_group_size_y
      - .offset:         72
        .size:           2
        .value_kind:     hidden_group_size_z
      - .offset:         74
        .size:           2
        .value_kind:     hidden_remainder_x
      - .offset:         76
        .size:           2
        .value_kind:     hidden_remainder_y
      - .offset:         78
        .size:           2
        .value_kind:     hidden_remainder_z
      - .offset:         96
        .size:           8
        .value_kind:     hidden_global_offset_x
      - .offset:         104
        .size:           8
        .value_kind:     hidden_global_offset_y
      - .offset:         112
        .size:           8
        .value_kind:     hidden_global_offset_z
      - .offset:         120
        .size:           2
        .value_kind:     hidden_grid_dims
      - .offset:         176
        .size:           4
        .value_kind:     hidden_dynamic_lds_size
    .group_segment_fixed_size: 0
    .kernarg_segment_align: 8
    .kernarg_segment_size: 312
    .language:       OpenCL C
    .language_version:
      - 2
      - 0
    .max_flat_workgroup_size: 512
    .name:           _Z10k_phase_hmN3pg84GemmEPDF16_PKfi
    .private_segment_fixed_size: 0
    .sgpr_count:     68
    .sgpr_spill_count: 0
    .symbol:         _Z10k_phase_hmN3pg84GemmEPDF16_PKfi.kd
    .uniform_work_group_size: 1
    .uses_dynamic_stack: false
    .vgpr_count:     140
    .vgpr_spill_count: 0
    .wavefront_size: 64
  - .agpr_count:     0
    .args:
      - .offset:         0
        .size:           32
        .value_kind:     by_value
      - .address_space:  global
        .offset:         32
        .size:           8
        .value_kind:     global_buffer
      - .address_space:  global
        .offset:         40
        .size:           8
        .value_kind:     global_buffer
      - .offset:         48
        .size:           4
        .value_kind:     by_value
      - .offset:         56
        .size:           4
        .value_kind:     hidden_block_count_x
      - .offset:         60
        .size:           4
        .value_kind:     hidden_block_count_y
      - .offset:         64
        .size:           4
        .value_kind:     hidden_block_count_z
      - .offset:         68
        .size:           2
        .value_kind:     hidden_group_size_x
      - .offset:         70
        .size:           2
        .value_kind:     hidden_group_size_y
      - .offset:         72
        .size:           2
        .value_kind:     hidden_group_size_z
      - .offset:         74
        .size:           2
        .value_kind:     hidden_remainder_x
      - .offset:         76
        .size:           2
        .value_kind:     hidden_remainder_y
      - .offset:         78
        .size:           2
        .value_kind:     hidden_remainder_z
      - .offset:         96
        .size:           8
        .value_kind:     hidden_global_offset_x
      - .offset:         104
        .size:           8
        .value_kind:     hidden_global_offset_y
      - .offset:         112
        .size:           8
        .value_kind:     hidden_global_offset_z
      - .offset:         120
        .size:           2
        .value_kind:     hidden_grid_dims
      - .offset:         176
        .size:           4
        .value_kind:     hidden_dynamic_lds_size
    .group_segment_fixed_size: 0
    .kernarg_segment_align: 8
    .kernarg_segment_size: 312
    .language:       OpenCL C
    .language_version:
      - 2
      - 0
    .max_flat_workgroup_size: 512
    .name:           _Z10k_phase_qmN3pg84GemmEPDF16_PKfi
    .private_segment_fixed_size: 0
    .sgpr_count:     67
    .sgpr_spill_count: 0
    .symbol:         _Z10k_phase_qmN3pg84GemmEPDF16_PKfi.kd
    .uniform_work_group_size: 1
    .uses_dynamic_stack: false
    .vgpr_count:     102
    .vgpr_spill_count: 0
    .wavefront_size: 64
  - .agpr_count:     0
    .args:
      - .offset:         0
        .size:           288
        .value_kind:     by_value
    .group_segment_fixed_size: 16640
    .kernarg_segment_align: 8
    .kernarg_segment_size: 288
    .language:       OpenCL C
    .language_version:
      - 2
      - 0
    .max_flat_workgroup_size: 256
    .name:           _Z11prep_kernel8PrepArgs
    .private_segment_fixed_size: 0
    .sgpr_count:     26
    .sgpr_spill_count: 0
    .symbol:         _Z11prep_kernel8PrepArgs.kd
    .uniform_work_group_size: 1
    .uses_dynamic_stack: false
    .vgpr_count:     35
    .vgpr_spill_count: 0
    .wavefront_size: 64
  - .agpr_count:     0
    .args:
      - .actual_access:  read_only
        .address_space:  global
        .offset:         0
        .size:           8
        .value_kind:     global_buffer
      - .actual_access:  read_only
        .address_space:  global
        .offset:         8
        .size:           8
        .value_kind:     global_buffer
      - .actual_access:  read_only
        .address_space:  global
        .offset:         16
        .size:           8
        .value_kind:     global_buffer
      - .actual_access:  write_only
        .address_space:  global
        .offset:         24
        .size:           8
        .value_kind:     global_buffer
    .group_segment_fixed_size: 0
    .kernarg_segment_align: 8
    .kernarg_segment_size: 32
    .language:       OpenCL C
    .language_version:
      - 2
      - 0
    .max_flat_workgroup_size: 256
    .name:           _Z11leaf_kernelPKfS0_PKiPDF16_
    .private_segment_fixed_size: 0
    .sgpr_count:     18
    .sgpr_spill_count: 0
    .symbol:         _Z11leaf_kernelPKfS0_PKiPDF16_.kd
    .uniform_work_group_size: 1
    .uses_dynamic_stack: false
    .vgpr_count:     25
    .vgpr_spill_count: 0
    .wavefront_size: 64
  - .agpr_count:     248
    .args:
      - .actual_access:  read_only
        .address_space:  global
        .offset:         0
        .size:           8
        .value_kind:     global_buffer
      - .actual_access:  read_only
        .address_space:  global
        .offset:         8
        .size:           8
        .value_kind:     global_buffer
      - .actual_access:  write_only
        .address_space:  global
        .offset:         16
        .size:           8
        .value_kind:     global_buffer
      - .actual_access:  write_only
        .address_space:  global
        .offset:         24
        .size:           8
        .value_kind:     global_buffer
    .group_segment_fixed_size: 0
    .kernarg_segment_align: 8
    .kernarg_segment_size: 32
    .language:       OpenCL C
    .language_version:
      - 2
      - 0
    .max_flat_workgroup_size: 256
    .name:           _Z10rnn_kernelPKDF16_S0_PDF16_S1_
    .private_segment_fixed_size: 0
    .sgpr_count:     22
    .sgpr_spill_count: 0
    .symbol:         _Z10rnn_kernelPKDF16_S0_PDF16_S1_.kd
    .uniform_work_group_size: 1
    .uses_dynamic_stack: false
    .vgpr_count:     496
    .vgpr_spill_count: 0
    .wavefront_size: 64
  - .agpr_count:     0
    .args:
      - .actual_access:  read_only
        .address_space:  global
        .offset:         0
        .size:           8
        .value_kind:     global_buffer
      - .actual_access:  read_only
        .address_space:  global
        .offset:         8
        .size:           8
        .value_kind:     global_buffer
      - .actual_access:  write_only
        .address_space:  global
        .offset:         16
        .size:           8
        .value_kind:     global_buffer
    .group_segment_fixed_size: 0
    .kernarg_segment_align: 8
    .kernarg_segment_size: 24
    .language:       OpenCL C
    .language_version:
      - 2
      - 0
    .max_flat_workgroup_size: 256
    .name:           _Z10max_kernelPKDF16_S0_PDF16_
    .private_segment_fixed_size: 0
    .sgpr_count:     18
    .sgpr_spill_count: 0
    .symbol:         _Z10max_kernelPKDF16_S0_PDF16_.kd
    .uniform_work_group_size: 1
    .uses_dynamic_stack: false
    .vgpr_count:     38
    .vgpr_spill_count: 0
    .wavefront_size: 64
  - .agpr_count:     0
    .args:
      - .actual_access:  read_only
        .address_space:  global
        .offset:         0
        .size:           8
        .value_kind:     global_buffer
      - .actual_access:  read_only
        .address_space:  global
        .offset:         8
        .size:           8
        .value_kind:     global_buffer
      - .actual_access:  read_only
        .address_space:  global
        .offset:         16
        .size:           8
        .value_kind:     global_buffer
      - .actual_access:  write_only
        .address_space:  global
        .offset:         24
        .size:           8
        .value_kind:     global_buffer
    .group_segment_fixed_size: 0
    .kernarg_segment_align: 8
    .kernarg_segment_size: 32
    .language:       OpenCL C
    .language_version:
      - 2
      - 0
    .max_flat_workgroup_size: 256
    .name:           _Z12final_kernelPKfS0_S0_Pf
    .private_segment_fixed_size: 0
    .sgpr_count:     14
    .sgpr_spill_count: 0
    .symbol:         _Z12final_kernelPKfS0_S0_Pf.kd
    .uniform_work_group_size: 1
    .uses_dynamic_stack: false
    .vgpr_count:     23
    .vgpr_spill_count: 0
    .wavefront_size: 64
  - .agpr_count:     0
    .args:
      - .address_space:  global
        .offset:         0
        .size:           8
        .value_kind:     global_buffer
      - .offset:         8
        .size:           4
        .value_kind:     by_value
      - .address_space:  global
        .offset:         16
        .size:           8
        .value_kind:     global_buffer
      - .offset:         24
        .size:           4
        .value_kind:     by_value
      - .actual_access:  write_only
        .address_space:  global
        .offset:         32
        .size:           8
        .value_kind:     global_buffer
      - .offset:         40
        .size:           4
        .value_kind:     by_value
      - .actual_access:  read_only
        .address_space:  global
        .offset:         48
        .size:           8
        .value_kind:     global_buffer
    .group_segment_fixed_size: 73728
    .kernarg_segment_align: 8
    .kernarg_segment_size: 56
    .language:       OpenCL C
    .language_version:
      - 2
      - 0
    .max_flat_workgroup_size: 512
    .name:           _Z9tg_kernelILi64ELi8ELi3ELb0EEvPKDF16_iS1_iPviPKf
    .private_segment_fixed_size: 0
    .sgpr_count:     38
    .sgpr_spill_count: 0
    .symbol:         _Z9tg_kernelILi64ELi8ELi3ELb0EEvPKDF16_iS1_iPviPKf.kd
    .uniform_work_group_size: 1
    .uses_dynamic_stack: false
    .vgpr_count:     128
    .vgpr_spill_count: 0
    .wavefront_size: 64
  - .agpr_count:     0
    .args:
      - .offset:         0
        .size:           32
        .value_kind:     by_value
      - .offset:         32
        .size:           32
        .value_kind:     by_value
      - .offset:         64
        .size:           16
        .value_kind:     by_value
      - .offset:         80
        .size:           24
        .value_kind:     by_value
      - .offset:         104
        .size:           24
        .value_kind:     by_value
      - .offset:         128
        .size:           4
        .value_kind:     hidden_block_count_x
      - .offset:         132
        .size:           4
        .value_kind:     hidden_block_count_y
      - .offset:         136
        .size:           4
        .value_kind:     hidden_block_count_z
      - .offset:         140
        .size:           2
        .value_kind:     hidden_group_size_x
      - .offset:         142
        .size:           2
        .value_kind:     hidden_group_size_y
      - .offset:         144
        .size:           2
        .value_kind:     hidden_group_size_z
      - .offset:         146
        .size:           2
        .value_kind:     hidden_remainder_x
      - .offset:         148
        .size:           2
        .value_kind:     hidden_remainder_y
      - .offset:         150
        .size:           2
        .value_kind:     hidden_remainder_z
      - .offset:         168
        .size:           8
        .value_kind:     hidden_global_offset_x
      - .offset:         176
        .size:           8
        .value_kind:     hidden_global_offset_y
      - .offset:         184
        .size:           8
        .value_kind:     hidden_global_offset_z
      - .offset:         192
        .size:           2
        .value_kind:     hidden_grid_dims
      - .offset:         248
        .size:           4
        .value_kind:     hidden_dynamic_lds_size
    .group_segment_fixed_size: 0
    .kernarg_segment_align: 8
    .kernarg_segment_size: 384
    .language:       OpenCL C
    .language_version:
      - 2
      - 0
    .max_flat_workgroup_size: 512
    .name:           _Z14k_phase_gen_utIN3pg86EpiH16ILb0ELb1EEENS1_ILb1ELb0EEEEvNS0_4GemmES4_NS0_6GenSrcET_T0_
    .private_segment_fixed_size: 0
    .sgpr_count:     89
    .sgpr_spill_count: 0
    .symbol:         _Z14k_phase_gen_utIN3pg86EpiH16ILb0ELb1EEENS1_ILb1ELb0EEEEvNS0_4GemmES4_NS0_6GenSrcET_T0_.kd
    .uniform_work_group_size: 1
    .uses_dynamic_stack: false
    .vgpr_count:     252
    .vgpr_spill_count: 0
    .wavefront_size: 64
  - .agpr_count:     0
    .args:
      - .address_space:  global
        .offset:         0
        .size:           8
        .value_kind:     global_buffer
      - .offset:         8
        .size:           4
        .value_kind:     by_value
      - .address_space:  global
        .offset:         16
        .size:           8
        .value_kind:     global_buffer
      - .offset:         24
        .size:           4
        .value_kind:     by_value
      - .actual_access:  write_only
        .address_space:  global
        .offset:         32
        .size:           8
        .value_kind:     global_buffer
      - .offset:         40
        .size:           4
        .value_kind:     by_value
      - .actual_access:  read_only
        .address_space:  global
        .offset:         48
        .size:           8
        .value_kind:     global_buffer
      - .offset:         56
        .size:           4
        .value_kind:     hidden_block_count_x
      - .offset:         60
        .size:           4
        .value_kind:     hidden_block_count_y
      - .offset:         64
        .size:           4
        .value_kind:     hidden_block_count_z
      - .offset:         68
        .size:           2
        .value_kind:     hidden_group_size_x
      - .offset:         70
        .size:           2
        .value_kind:     hidden_group_size_y
      - .offset:         72
        .size:           2
        .value_kind:     hidden_group_size_z
      - .offset:         74
        .size:           2
        .value_kind:     hidden_remainder_x
      - .offset:         76
        .size:           2
        .value_kind:     hidden_remainder_y
      - .offset:         78
        .size:           2
        .value_kind:     hidden_remainder_z
      - .offset:         96
        .size:           8
        .value_kind:     hidden_global_offset_x
      - .offset:         104
        .size:           8
        .value_kind:     hidden_global_offset_y
      - .offset:         112
        .size:           8
        .value_kind:     hidden_global_offset_z
      - .offset:         120
        .size:           2
        .value_kind:     hidden_grid_dims
      - .offset:         176
        .size:           4
        .value_kind:     hidden_dynamic_lds_size
    .group_segment_fixed_size: 0
    .kernarg_segment_align: 8
    .kernarg_segment_size: 312
    .language:       OpenCL C
    .language_version:
      - 2
      - 0
    .max_flat_workgroup_size: 512
    .name:           _Z9tg_kernelILi128ELi8ELi1ELb1EEvPKDF16_iS1_iPviPKf
    .private_segment_fixed_size: 0
    .sgpr_count:     25
    .sgpr_spill_count: 0
    .symbol:         _Z9tg_kernelILi128ELi8ELi1ELb1EEvPKDF16_iS1_iPviPKf.kd
    .uniform_work_group_size: 1
    .uses_dynamic_stack: false
    .vgpr_count:     96
    .vgpr_spill_count: 0
    .wavefront_size: 64
  - .agpr_count:     0
    .args:
      - .address_space:  global
        .offset:         0
        .size:           8
        .value_kind:     global_buffer
      - .offset:         8
        .size:           4
        .value_kind:     by_value
      - .address_space:  global
        .offset:         16
        .size:           8
        .value_kind:     global_buffer
      - .offset:         24
        .size:           4
        .value_kind:     by_value
      - .actual_access:  write_only
        .address_space:  global
        .offset:         32
        .size:           8
        .value_kind:     global_buffer
      - .offset:         40
        .size:           4
        .value_kind:     by_value
      - .actual_access:  read_only
        .address_space:  global
        .offset:         48
        .size:           8
        .value_kind:     global_buffer
    .group_segment_fixed_size: 73728
    .kernarg_segment_align: 8
    .kernarg_segment_size: 56
    .language:       OpenCL C
    .language_version:
      - 2
      - 0
    .max_flat_workgroup_size: 512
    .name:           _Z9tg_kernelILi64ELi8ELi1ELb0EEvPKDF16_iS1_iPviPKf
    .private_segment_fixed_size: 0
    .sgpr_count:     38
    .sgpr_spill_count: 0
    .symbol:         _Z9tg_kernelILi64ELi8ELi1ELb0EEvPKDF16_iS1_iPviPKf.kd
    .uniform_work_group_size: 1
    .uses_dynamic_stack: false
    .vgpr_count:     128
    .vgpr_spill_count: 0
    .wavefront_size: 64
  - .agpr_count:     0
    .args:
      - .address_space:  global
        .offset:         0
        .size:           8
        .value_kind:     global_buffer
      - .offset:         8
        .size:           4
        .value_kind:     by_value
      - .address_space:  global
        .offset:         16
        .size:           8
        .value_kind:     global_buffer
      - .offset:         24
        .size:           4
        .value_kind:     by_value
      - .actual_access:  write_only
        .address_space:  global
        .offset:         32
        .size:           8
        .value_kind:     global_buffer
      - .offset:         40
        .size:           4
        .value_kind:     by_value
      - .actual_access:  read_only
        .address_space:  global
        .offset:         48
        .size:           8
        .value_kind:     global_buffer
    .group_segment_fixed_size: 73728
    .kernarg_segment_align: 8
    .kernarg_segment_size: 56
    .language:       OpenCL C
    .language_version:
      - 2
      - 0
    .max_flat_workgroup_size: 512
    .name:           _Z9tg_kernelILi64ELi8ELi4ELb0EEvPKDF16_iS1_iPviPKf
    .private_segment_fixed_size: 0
    .sgpr_count:     38
    .sgpr_spill_count: 0
    .symbol:         _Z9tg_kernelILi64ELi8ELi4ELb0EEvPKDF16_iS1_iPviPKf.kd
    .uniform_work_group_size: 1
    .uses_dynamic_stack: false
    .vgpr_count:     128
    .vgpr_spill_count: 0
    .wavefront_size: 64
  - .agpr_count:     0
    .args:
      - .address_space:  global
        .offset:         0
        .size:           8
        .value_kind:     global_buffer
      - .offset:         8
        .size:           4
        .value_kind:     by_value
      - .address_space:  global
        .offset:         16
        .size:           8
        .value_kind:     global_buffer
      - .offset:         24
        .size:           4
        .value_kind:     by_value
      - .actual_access:  write_only
        .address_space:  global
        .offset:         32
        .size:           8
        .value_kind:     global_buffer
      - .offset:         40
        .size:           4
        .value_kind:     by_value
      - .actual_access:  read_only
        .address_space:  global
        .offset:         48
        .size:           8
        .value_kind:     global_buffer
    .group_segment_fixed_size: 73728
    .kernarg_segment_align: 8
    .kernarg_segment_size: 56
    .language:       OpenCL C
    .language_version:
      - 2
      - 0
    .max_flat_workgroup_size: 512
    .name:           _Z9tg_kernelILi64ELi8ELi2ELb0EEvPKDF16_iS1_iPviPKf
    .private_segment_fixed_size: 0
    .sgpr_count:     38
    .sgpr_spill_count: 0
    .symbol:         _Z9tg_kernelILi64ELi8ELi2ELb0EEvPKDF16_iS1_iPviPKf.kd
    .uniform_work_group_size: 1
    .uses_dynamic_stack: false
    .vgpr_count:     128
    .vgpr_spill_count: 0
    .wavefront_size: 64
